# expert-weight conversion removed from P1 and staggered: group pair k converts at the start of P2/P3/P4/SEAM5 (memory-bound conversion of 2 XCDs overlaps the other 6 XCDs' GEMM); P9 epilogue prefetch
# baseline (speedup 1.0000x reference)
; __global__ void __launch_bounds__(NWAVES * 64, 2) mk_fwd(Args args) {
;     ...
;         {
;             const int step = G * NWAVES; int it0 = CONV_EARLY + bid * NWAVES + wave;
;             ConvDesc dA, dB; f32x4 vA[16], vB[16];
;             if (it0 < NCONV_ITEMS) { CONV_DECODE(dA, it0); conv_load(vA, dA, lane); }
.Lconv_entry:
	s_cmp_eq_u32 s99, 0
	s_cbranch_scc0 .Lconv_go
	v_mbcnt_lo_u32_b32 v64, -1, 0
	v_mbcnt_hi_u32_b32 v64, -1, v64
	s_lshl_b32 s50, s83, 5
	v_lshlrev_b32_e32 v132, 2, v64
	s_branch .LBB0_739

; #define KIN(i) ((const float*)(GAS const float*)karg()[i])
; #define WSP(type, off) ((type*)(KWS() + (off)))
; #define CBID() (LOCAL_OK() ? ((bid & 7) * 32 + (bid >> 3)) : bid)
; __global__ void __launch_bounds__(NWAVES * 64, 2) mk_fwd(Args args) {
;     ...
;         const float* x = KIN(0); const float* norm_mix_g = KIN(2); const float* mod = WSP(float, WS_MOD); bf16_t* xn = WSP(bf16_t, WS_XN);
;         for (int w0 = (CBID() * 8 + wave) * 32; w0 < T; w0 += G * 8 * 32) {
;             const float* mb = mod + (size_t)(w0 >> 12) * 6144;
;             ModV mv; mod_load(mv, norm_mix_g, mb + 0, mb + 1024, lane);
;             RowV ring[4];
; #pragma unroll
;             for (int d = 0; d < 4; ++d) row_load(ring[d], x + (size_t)(w0 + d) * D, lane);
.LBB0_739:
	s_cmp_eq_u32 s99, 1
	s_cbranch_scc1 .Lslot_ret1
	s_cmp_eq_u32 s99, 2
	s_cbranch_scc1 .Lslot_ret2
	s_cmp_eq_u32 s99, 3
	s_cbranch_scc1 .Lslot_ret3
	s_cmp_eq_u32 s99, 4
	s_cbranch_scc1 .Lslot_ret4
	s_cmpk_lg_i32 s33, 0x100
	s_cselect_b64 s[0:1], -1, 0
	v_writelane_b32 v251, s0, 9
	s_and_b32 s54, s50, 0xe0
	s_mov_b64 s[8:9], s[78:79]
	v_writelane_b32 v251, s1, 10
	s_lshr_b32 s0, s83, 3
	s_add_i32 s6, s54, s0
	s_cmpk_eq_i32 s33, 0x100
	s_cselect_b64 s[2:3], -1, 0
	s_and_b64 s[0:1], s[2:3], exec
	s_cselect_b32 s0, s6, s83
	s_lshl_b32 s0, s0, 8
	s_lshl_b32 s96, s85, 5
	s_add_i32 s6, s0, s96
	s_lshl_b32 s0, s33, 8
	v_writelane_b32 v251, s0, 11
	s_cmp_gt_i32 s6, 0xffff
	s_mov_b64 s[10:11], s[78:79]
	v_writelane_b32 v251, s1, 12
	s_mov_b64 s[0:1], s[78:79]
	s_mov_b64 s[12:13], s[78:79]
	s_cbranch_scc1 .LBB0_754
	s_load_dwordx2 s[14:15], s[10:11], 0xa0
	s_load_dwordx2 s[16:17], s[0:1], 0x0
	s_load_dwordx2 s[20:21], s[8:9], 0x10
	s_load_dwordx2 s[22:23], s[12:13], 0xa0
	v_ashrrev_i32_e32 v133, 31, v132
	s_waitcnt vmcnt(15)
	v_lshlrev_b64 v[0:1], 2, v[132:133]
	s_waitcnt lgkmcnt(0)
	s_add_u32 s18, s14, 0x100000
	v_lshl_add_u64 v[96:97], s[20:21], 0, v[0:1]
	v_lshl_add_u64 v[98:99], s[16:17], 0, v[0:1]
	v_lshlrev_b64 v[0:1], 1, v[132:133]
	s_addc_u32 s19, s15, 0
	v_lshl_add_u64 v[2:3], s[22:23], 0, v[0:1]
	s_mov_b64 s[0:1], 0x10000000
	s_ashr_i32 s7, s6, 31
	v_lshl_add_u64 v[100:101], v[2:3], 0, s[0:1]
	s_lshl_b64 s[0:1], s[6:7], 11
	s_add_u32 s0, s22, s0
	s_addc_u32 s1, s23, s1
	v_lshl_add_u64 v[0:1], s[0:1], 0, v[0:1]
	s_mov_b64 s[0:1], 0x10000400
	v_lshl_add_u64 v[102:103], v[0:1], 0, s[0:1]
	v_readlane_b32 s0, v251, 11
	v_readlane_b32 s1, v251, 12
	s_mov_b32 s8, s0
	s_ashr_i32 s9, s0, 31
	v_writelane_b32 v251, s0, 11
	s_lshl_b64 s[8:9], s[8:9], 11
	s_mov_b64 s[10:11], 0x1000
	v_mov_b32_e32 v122, 0x358637bd
	s_mov_b64 s[12:13], 0x2000
	v_writelane_b32 v251, s1, 12
	s_branch .LBB0_742

; #define WSP(type, off) ((type*)(KWS() + (off)))
; __global__ void __launch_bounds__(NWAVES * 64, 2) mk_fwd(Args args) {
;     ...
;     for (int rep_ = 0; rep_ < REPS(2); ++rep_) if (IN(2)) { bf16_t* xn = WSP(bf16_t, WS_XN); bf16_t* WZ = WSP(bf16_t, WS_WZ); bf16_t* zb = WSP(bf16_t, WS_Z);
;         pg8::Gemm g{xn, WZ, T, 2048, 1024}; pg8::StaticOrder S; S.init(T, 2048, G, bid); pg8::EpiPair<false> E{zb, D};
;         pg8::gemm_phase<pg8::EpiPair<false>, pg8::StaticOrder, pg8::APlain, true, true>(lds, g, S, E, pg8::APlain{}, wave); }
.LBB0_834:
	s_bfe_u32 s98, s83, 0x20001
	s_cmp_eq_u32 s98, 0
	s_cbranch_scc1 .Lslot_do1
	s_branch .Lslot_go1
.Lslot_do1:
	s_mov_b32 s99, 1
	s_mov_b32 s100, s54
	v_writelane_b32 v252, s2, 0
	v_writelane_b32 v252, s3, 1
	v_writelane_b32 v252, s16, 2
	v_writelane_b32 v252, s17, 3
	v_writelane_b32 v252, s18, 4
	v_writelane_b32 v252, s19, 5
	v_writelane_b32 v252, s20, 6
	v_writelane_b32 v252, s21, 7
	v_writelane_b32 v252, s23, 8
	v_writelane_b32 v252, s24, 9
	v_writelane_b32 v252, s25, 10
	v_writelane_b32 v252, s26, 11
	v_writelane_b32 v252, s40, 12
	v_writelane_b32 v252, s42, 13
	v_mov_b32_e32 v253, v3
	v_mov_b32_e32 v254, v5
	s_mov_b64 s[0:1], s[78:79]
	s_lshl_b32 s2, s33, 9
	s_mul_i32 s3, s85, 0x4100
	s_lshl_b32 s48, s33, 3
	s_lshl_b32 s49, s83, 9
	s_lshl_b32 s50, s83, 3
	s_add_i32 s50, s50, s85
	s_lshl_b32 s88, s85, 6
	s_branch .Lconv_entry
.Lslot_ret1:
	s_mov_b32 s54, s100
	v_readlane_b32 s2, v252, 0
	v_readlane_b32 s3, v252, 1
	v_readlane_b32 s16, v252, 2
	v_readlane_b32 s17, v252, 3
	v_readlane_b32 s18, v252, 4
	v_readlane_b32 s19, v252, 5
	v_readlane_b32 s20, v252, 6
	v_readlane_b32 s21, v252, 7
	v_readlane_b32 s23, v252, 8
	v_readlane_b32 s24, v252, 9
	v_readlane_b32 s25, v252, 10
	v_readlane_b32 s26, v252, 11
	v_readlane_b32 s40, v252, 12
	v_readlane_b32 s42, v252, 13
	v_mov_b32_e32 v3, v253
	v_mov_b32_e32 v5, v254
	s_nop 4
	s_waitcnt vmcnt(0) lgkmcnt(0)
	s_barrier

; #define KIN(i) ((const float*)(GAS const float*)karg()[i])
; #define WSP(type, off) ((type*)(KWS() + (off)))
; __global__ void __launch_bounds__(NWAVES * 64, 2) mk_fwd(Args args) {
;     ...
;     for (int rep_ = 0; rep_ < REPS(3); ++rep_) if (IN(3)) { bf16_t* xn = WSP(bf16_t, WS_XN); bf16_t* WB = WSP(bf16_t, WS_WB); bf16_t* zb = WSP(bf16_t, WS_Z); bf16_t* ypre = WSP(bf16_t, WS_YPRE); const float* conv_w = KIN(7);
;         pg8::Gemm g{xn, WB, T, 1024, 1024}; pg8::StaticOrder S; S.init(T, 1024, G, bid); pg8::EpiYpre E{ypre, zb, conv_w};
;         pg8::gemm_phase<pg8::EpiYpre, pg8::StaticOrder, pg8::APlain, true, true>(lds, g, S, E, pg8::APlain{}, wave); }
.LBB0_934:
	s_bfe_u32 s98, s83, 0x20001
	s_cmp_eq_u32 s98, 1
	s_cbranch_scc1 .Lslot_do2
	s_branch .Lslot_go2
.Lslot_do2:
	s_mov_b32 s99, 2
	s_mov_b32 s100, s54
	v_writelane_b32 v252, s2, 0
	v_writelane_b32 v252, s3, 1
	v_writelane_b32 v252, s16, 2
	v_writelane_b32 v252, s17, 3
	v_writelane_b32 v252, s18, 4
	v_writelane_b32 v252, s19, 5
	v_writelane_b32 v252, s20, 6
	v_writelane_b32 v252, s21, 7
	v_writelane_b32 v252, s23, 8
	v_writelane_b32 v252, s24, 9
	v_writelane_b32 v252, s25, 10
	v_writelane_b32 v252, s26, 11
	v_writelane_b32 v252, s40, 12
	v_writelane_b32 v252, s42, 13
	v_mov_b32_e32 v253, v3
	v_mov_b32_e32 v254, v5
	s_mov_b64 s[0:1], s[78:79]
	s_lshl_b32 s2, s33, 9
	s_mul_i32 s3, s85, 0x4100
	s_lshl_b32 s48, s33, 3
	s_lshl_b32 s49, s83, 9
	s_lshl_b32 s50, s83, 3
	s_add_i32 s50, s50, s85
	s_lshl_b32 s88, s85, 6
	s_branch .Lconv_entry

; #define KIN(i) ((const float*)(GAS const float*)karg()[i])
; #define KOUT() ((float*)(GAS float*)karg()[19])
; #define WSP(type, off) ((type*)(KWS() + (off)))
; __global__ void __launch_bounds__(NWAVES * 64, 2) mk_fwd(Args args) {
;     ...
;     for (int rep_ = 0; rep_ < REPS(4); ++rep_) if (IN(4)) { bf16_t* ypre = WSP(bf16_t, WS_YPRE); bf16_t* WCO = WSP(bf16_t, WS_WCO); bf16_t* xr = (bf16_t*)KOUT(); const float* x = KIN(0); const float* mod = WSP(float, WS_MOD);
;         pg8::Gemm g{ypre, WCO, T, 1024, 1024}; pg8::StaticOrder S; S.init(T, 1024, G, bid); pg8::EpiRes<true> E{xr, x, mod + 2048};
;         pg8::gemm_phase<pg8::EpiRes<true>, pg8::StaticOrder, pg8::APlain, true, true>(lds, g, S, E, pg8::APlain{}, wave); }
.LBB0_1042:
	s_bfe_u32 s98, s83, 0x20001
	s_cmp_eq_u32 s98, 2
	s_cbranch_scc1 .Lslot_do3
	s_branch .Lslot_go3
.Lslot_do3:
	s_mov_b32 s99, 3
	s_mov_b32 s100, s54
	v_writelane_b32 v252, s2, 0
	v_writelane_b32 v252, s3, 1
	v_writelane_b32 v252, s16, 2
	v_writelane_b32 v252, s17, 3
	v_writelane_b32 v252, s18, 4
	v_writelane_b32 v252, s19, 5
	v_writelane_b32 v252, s20, 6
	v_writelane_b32 v252, s21, 7
	v_writelane_b32 v252, s23, 8
	v_writelane_b32 v252, s24, 9
	v_writelane_b32 v252, s25, 10
	v_writelane_b32 v252, s26, 11
	v_writelane_b32 v252, s40, 12
	v_writelane_b32 v252, s42, 13
	v_mov_b32_e32 v253, v3
	v_mov_b32_e32 v254, v5
	s_mov_b64 s[0:1], s[78:79]
	s_lshl_b32 s2, s33, 9
	s_mul_i32 s3, s85, 0x4100
	s_lshl_b32 s48, s33, 3
	s_lshl_b32 s49, s83, 9
	s_lshl_b32 s50, s83, 3
	s_add_i32 s50, s50, s85
	s_lshl_b32 s88, s85, 6
	s_branch .Lconv_entry
.Lslot_ret3:
	s_mov_b32 s54, s100
	v_readlane_b32 s2, v252, 0
	v_readlane_b32 s3, v252, 1
	v_readlane_b32 s16, v252, 2
	v_readlane_b32 s17, v252, 3
	v_readlane_b32 s18, v252, 4
	v_readlane_b32 s19, v252, 5
	v_readlane_b32 s20, v252, 6
	v_readlane_b32 s21, v252, 7
	v_readlane_b32 s23, v252, 8
	v_readlane_b32 s24, v252, 9
	v_readlane_b32 s25, v252, 10
	v_readlane_b32 s26, v252, 11
	v_readlane_b32 s40, v252, 12
	v_readlane_b32 s42, v252, 13
	v_mov_b32_e32 v3, v253
	v_mov_b32_e32 v5, v254
	s_nop 4
	s_waitcnt vmcnt(0) lgkmcnt(0)
	s_barrier
	s_cmpk_lt_i32 s83, 0x400
	s_cselect_b64 s[20:21], -1, 0

; #define KIN(i) ((const float*)(GAS const float*)karg()[i])
; #define KOUT() ((float*)(GAS float*)karg()[19])
; #define KWS() ((unsigned char*)(GAS unsigned char*)karg()[20])
; #define WSP(type, off) ((type*)(KWS() + (off)))
; #define CBID() (LOCAL_OK() ? ((bid & 7) * 32 + (bid >> 3)) : bid)
; #define SEAM(k) do { if (IN(k) && IN((k) + 1)) GRID_BAR(); } while (0)
; #define MODL() (WSP(float, WS_MOD) + (size_t)l * 16 * 6144)
; #define CNTL() (WSP(int, WS_CTL) + 64 * l)
; #define MODL() (WSP(float, WS_MOD) + (size_t)l * 16 * 6144)
; #define CNTL() (WSP(int, WS_CTL) + 64 * l)
; __global__ void __launch_bounds__(NWAVES * 64, 2) mk_fwd(Args args) {
;     ...
;         if (IN(pb0)) rt::router_phase(lds, (const bf16_t*)KOUT(), WSP(bf16_t, WS_XN), KIN(3) + l * D, MODL(), KIN(11) + (size_t)l * D * 4, KIN(12) + l * 4, KIN(13) + (size_t)l * 4 * D * 8, KIN(14) + l * 32,
;                                       CNTL(), WSP(int, WS_LTOK), WSP(float, WS_LW), WSP(int, WS_TSLOT), CBID(), G, wave, LOCAL_OK() ? (const unsigned char*)(KWS() + WS_RTAB + (size_t)l * 16 * RTAB_STRIDE) : nullptr);
;         SEAM(pb0);
.LBB0_1380:
	s_bfe_u32 s98, s83, 0x20001
	s_cmp_eq_u32 s98, 3
	s_cbranch_scc1 .Lslot_do4
	s_branch .Lslot_go4
.Lslot_do4:
	s_mov_b32 s99, 4
	s_mov_b32 s100, s54
	v_writelane_b32 v252, s2, 0
	v_writelane_b32 v252, s3, 1
	v_writelane_b32 v252, s16, 2
	v_writelane_b32 v252, s17, 3
	v_writelane_b32 v252, s18, 4
	v_writelane_b32 v252, s19, 5
	v_writelane_b32 v252, s20, 6
	v_writelane_b32 v252, s21, 7
	v_writelane_b32 v252, s23, 8
	v_writelane_b32 v252, s24, 9
	v_writelane_b32 v252, s25, 10
	v_writelane_b32 v252, s26, 11
	v_writelane_b32 v252, s40, 12
	v_writelane_b32 v252, s42, 13
	v_mov_b32_e32 v253, v3
	v_mov_b32_e32 v254, v5
	s_mov_b64 s[0:1], s[78:79]
	s_lshl_b32 s2, s33, 9
	s_mul_i32 s3, s85, 0x4100
	s_lshl_b32 s48, s33, 3
	s_lshl_b32 s49, s83, 9
	s_lshl_b32 s50, s83, 3
	s_add_i32 s50, s50, s85
	s_lshl_b32 s88, s85, 6
	s_branch .Lconv_entry

; __global__ void __launch_bounds__(NWAVES * 64, 2) mk_fwd(Args args) {
	.amdhsa_kernel _Z6mk_fwd4Args
		.amdhsa_group_segment_fixed_size 0
		.amdhsa_private_segment_fixed_size 0
		.amdhsa_kernarg_size 432
		.amdhsa_user_sgpr_count 2
		.amdhsa_user_sgpr_dispatch_ptr 0
		.amdhsa_user_sgpr_queue_ptr 0
		.amdhsa_user_sgpr_kernarg_segment_ptr 1
		.amdhsa_user_sgpr_dispatch_id 0
		.amdhsa_user_sgpr_kernarg_preload_length 0
		.amdhsa_user_sgpr_kernarg_preload_offset 0
		.amdhsa_user_sgpr_private_segment_size 0
		.amdhsa_uses_dynamic_stack 0
		.amdhsa_enable_private_segment 0
		.amdhsa_system_sgpr_workgroup_id_x 1
		.amdhsa_system_sgpr_workgroup_id_y 0
		.amdhsa_system_sgpr_workgroup_id_z 0
		.amdhsa_system_sgpr_workgroup_info 0
		.amdhsa_system_vgpr_workitem_id 0
		.amdhsa_next_free_vgpr 256
		.amdhsa_next_free_sgpr 102
		.amdhsa_accum_offset 256
		.amdhsa_reserve_vcc 1
		.amdhsa_float_round_mode_32 0
		.amdhsa_float_round_mode_16_64 0
		.amdhsa_float_denorm_mode_32 3
		.amdhsa_float_denorm_mode_16_64 3
		.amdhsa_dx10_clamp 1
		.amdhsa_ieee_mode 1
		.amdhsa_fp16_overflow 0
		.amdhsa_tg_split 0
		.amdhsa_exception_fp_ieee_invalid_op 0
		.amdhsa_exception_fp_denorm_src 0
		.amdhsa_exception_fp_ieee_div_zero 0
		.amdhsa_exception_fp_ieee_overflow 0
		.amdhsa_exception_fp_ieee_underflow 0
		.amdhsa_exception_fp_ieee_inexact 0
		.amdhsa_exception_int_div_zero 0
	.end_amdhsa_kernel

; __global__ void __launch_bounds__(NWAVES * 64, 2) mk_fwd(Args args) {
amdhsa.kernels:
  - .agpr_count:     0
    .args:
      - .offset:         0
        .size:           176
        .value_kind:     by_value
      - .offset:         176
        .size:           4
        .value_kind:     hidden_block_count_x
      - .offset:         180
        .size:           4
        .value_kind:     hidden_block_count_y
      - .offset:         184
        .size:           4
        .value_kind:     hidden_block_count_z
      - .offset:         188
        .size:           2
        .value_kind:     hidden_group_size_x
      - .offset:         190
        .size:           2
        .value_kind:     hidden_group_size_y
      - .offset:         192
        .size:           2
        .value_kind:     hidden_group_size_z
      - .offset:         194
        .size:           2
        .value_kind:     hidden_remainder_x
      - .offset:         196
        .size:           2
        .value_kind:     hidden_remainder_y
      - .offset:         198
        .size:           2
        .value_kind:     hidden_remainder_z
      - .offset:         216
        .size:           8
        .value_kind:     hidden_global_offset_x
      - .offset:         224
        .size:           8
        .value_kind:     hidden_global_offset_y
      - .offset:         232
        .size:           8
        .value_kind:     hidden_global_offset_z
      - .offset:         240
        .size:           2
        .value_kind:     hidden_grid_dims
      - .offset:         296
        .size:           4
        .value_kind:     hidden_dynamic_lds_size
    .group_segment_fixed_size: 0
    .kernarg_segment_align: 8
    .kernarg_segment_size: 432
    .language:       OpenCL C
    .language_version:
      - 2
      - 0
    .max_flat_workgroup_size: 512
    .name:           _Z6mk_fwd4Args
    .private_segment_fixed_size: 0
    .sgpr_count:     108
    .sgpr_spill_count: 357
    .symbol:         _Z6mk_fwd4Args.kd
    .uniform_work_group_size: 1
    .uses_dynamic_stack: false
    .vgpr_count:     256
    .vgpr_spill_count: 0
    .wavefront_size: 64
